# no s_setprio anywhere (static raise removed too), otherwise v048
# speedup vs baseline: 1.0017x; 1.0017x over previous
_Z6mk_fwd4Args:
	s_load_dword s3, s[0:1], 0xb8
	s_add_u32 s4, s0, 0xb8
	s_addc_u32 s5, s1, 0
	v_readfirstlane_b32 s52, v0
	v_writelane_b32 v252, s4, 0
	s_nop 1
	v_writelane_b32 v252, s5, 1
	s_waitcnt lgkmcnt(0)
	s_cmp_lt_u32 s52, 0x100
	s_cbranch_scc1 .Lprio_skip
.Lprio_skip:
	s_and_b32 s4, s3, 7
	s_cmp_lg_u32 s4, 0
	v_writelane_b32 v252, s2, 2
	s_cbranch_scc1 .LBB0_2
	s_ashr_i32 s5, s2, 31
	s_lshr_b32 s5, s5, 29
	s_add_i32 s5, s2, s5
	s_and_b32 s6, s5, -8
	s_ashr_i32 s4, s3, 3
	s_sub_i32 s6, s2, s6
	s_mul_i32 s4, s4, s6
	s_ashr_i32 s5, s5, 3
	s_add_i32 s4, s4, s5
	v_writelane_b32 v252, s4, 2
